# SALU-only hoist in front of the K-loop segment barriers (scalar LDS-offset adds and the vcc mask and), VALU address ops and m0 writes left behind the barrier
# baseline (speedup 1.0000x reference)
.LBB0_285:
	ds_read_b128 v[18:21], v201
	ds_read_b128 v[22:25], v201 offset:1024
	ds_read_b128 v[26:29], v201 offset:2048
	ds_read_b128 v[30:33], v201 offset:3072
	ds_read_b128 v[2:5], v202
	ds_read_b128 v[6:9], v202 offset:1024
	ds_read_b128 v[10:13], v202 offset:2048
	ds_read_b128 v[14:17], v202 offset:3072
	s_add_u32 s62, s58, 0xfffc0080
	s_addc_u32 s63, s59, -1
	s_cmp_eq_u32 s71, 12
	s_cselect_b32 s67, s43, s63
	s_cselect_b32 s66, s57, s62
	s_cselect_b32 s63, s45, s70
	s_cselect_b32 s62, s68, s69
	v_lshl_add_u64 v[232:233], s[58:59], 0, v[172:173]
	s_add_i32 m0, s55, 0xc000
	ds_read_b128 v[176:179], v203
	ds_read_b128 v[180:183], v203 offset:1024
	ds_read_b128 v[206:209], v203 offset:2048
	ds_read_b128 v[210:213], v203 offset:3072
	ds_read_b128 v[214:217], v203 offset:4096
	ds_read_b128 v[218:221], v203 offset:5120
	ds_read_b128 v[222:225], v203 offset:6144
	ds_read_b128 v[226:229], v203 offset:7168
	global_load_lds_dwordx4 v[232:233], off
	v_lshl_add_u64 v[232:233], s[58:59], 0, v[174:175]
	s_add_i32 m0, s55, 0xe000
	s_nop 0
	global_load_lds_dwordx4 v[232:233], off
	s_waitcnt vmcnt(8)
	s_waitcnt lgkmcnt(0)
	s_barrier
	s_setprio 1
	s_waitcnt lgkmcnt(0)
	v_mfma_scale_f32_16x16x128_f8f6f4 v[158:161], v[18:25], v[176:183], v[158:161], v204, v204 op_sel_hi:[0,0,0]
	v_mfma_scale_f32_16x16x128_f8f6f4 v[154:157], v[26:33], v[176:183], v[154:157], v204, v204 op_sel_hi:[0,0,0]
	v_mfma_scale_f32_16x16x128_f8f6f4 v[150:153], v[18:25], v[206:213], v[150:153], v204, v204 op_sel_hi:[0,0,0]
	v_mfma_scale_f32_16x16x128_f8f6f4 v[146:149], v[26:33], v[206:213], v[146:149], v204, v204 op_sel_hi:[0,0,0]
	v_mfma_scale_f32_16x16x128_f8f6f4 v[130:133], v[18:25], v[214:221], v[130:133], v204, v204 op_sel_hi:[0,0,0]
	v_mfma_scale_f32_16x16x128_f8f6f4 v[122:125], v[26:33], v[214:221], v[122:125], v204, v204 op_sel_hi:[0,0,0]
	v_mfma_scale_f32_16x16x128_f8f6f4 v[118:121], v[18:25], v[222:229], v[118:121], v204, v204 op_sel_hi:[0,0,0]
	v_mfma_scale_f32_16x16x128_f8f6f4 v[114:117], v[26:33], v[222:229], v[114:117], v204, v204 op_sel_hi:[0,0,0]
	s_setprio 0
	s_setprio 1
	v_mfma_scale_f32_16x16x128_f8f6f4 v[142:145], v[2:9], v[176:183], v[142:145], v204, v204 op_sel_hi:[0,0,0]
	v_mfma_scale_f32_16x16x128_f8f6f4 v[138:141], v[10:17], v[176:183], v[138:141], v204, v204 op_sel_hi:[0,0,0]
	v_mfma_scale_f32_16x16x128_f8f6f4 v[134:137], v[2:9], v[206:213], v[134:137], v204, v204 op_sel_hi:[0,0,0]
	v_mfma_scale_f32_16x16x128_f8f6f4 v[126:129], v[10:17], v[206:213], v[126:129], v204, v204 op_sel_hi:[0,0,0]
	v_mfma_scale_f32_16x16x128_f8f6f4 v[110:113], v[2:9], v[214:221], v[110:113], v204, v204 op_sel_hi:[0,0,0]
	v_mfma_scale_f32_16x16x128_f8f6f4 v[106:109], v[10:17], v[214:221], v[106:109], v204, v204 op_sel_hi:[0,0,0]
	v_mfma_scale_f32_16x16x128_f8f6f4 v[102:105], v[2:9], v[222:229], v[102:105], v204, v204 op_sel_hi:[0,0,0]
	v_mfma_scale_f32_16x16x128_f8f6f4 v[98:101], v[10:17], v[222:229], v[98:101], v204, v204 op_sel_hi:[0,0,0]
	s_setprio 0
	s_add_i32 vcc_lo, s97, s39
	s_barrier
	v_lshl_add_u64 v[176:177], s[62:63], 0, v[164:165]
	s_mov_b32 m0, vcc_lo
	ds_read_b128 v[206:209], v203 offset:16384
	ds_read_b128 v[210:213], v203 offset:17408
	ds_read_b128 v[214:217], v203 offset:18432
	ds_read_b128 v[218:221], v203 offset:19456
	ds_read_b128 v[222:225], v203 offset:20480
	ds_read_b128 v[226:229], v203 offset:21504
	ds_read_b128 v[232:235], v203 offset:22528
	ds_read_b128 v[236:239], v203 offset:23552
	global_load_lds_dwordx4 v[176:177], off
	s_add_i32 m0, vcc_lo, 0x2000
	s_add_u32 vcc_lo, s62, 0x40000
	v_lshl_add_u64 v[178:179], s[62:63], 0, v[168:169]
	s_addc_u32 vcc_hi, s63, 0
	s_add_i32 s18, s34, s39
	global_load_lds_dwordx4 v[178:179], off
	v_lshl_add_u64 v[180:181], vcc, 0, v[164:165]
	s_mov_b32 m0, s18
	v_lshl_add_u64 v[182:183], s[66:67], 0, v[166:167]
	global_load_lds_dwordx4 v[180:181], off
	v_lshl_add_u64 v[180:181], vcc, 0, v[168:169]
	s_add_i32 m0, s18, 0x2000
	s_nop 0
	global_load_lds_dwordx4 v[180:181], off
	v_lshl_add_u64 v[180:181], s[66:67], 0, v[162:163]
	s_mov_b32 m0, s55
	s_nop 0
	global_load_lds_dwordx4 v[180:181], off
	s_mov_b32 m0, s90
	s_nop 0
	global_load_lds_dwordx4 v[182:183], off
	s_waitcnt vmcnt(8)
	s_waitcnt lgkmcnt(0)
	s_barrier
	s_setprio 1
	s_waitcnt lgkmcnt(0)
	v_mfma_scale_f32_16x16x128_f8f6f4 v[94:97], v[18:25], v[206:213], v[94:97], v204, v204 op_sel_hi:[0,0,0]
	v_mfma_scale_f32_16x16x128_f8f6f4 v[90:93], v[26:33], v[206:213], v[90:93], v204, v204 op_sel_hi:[0,0,0]
	v_mfma_scale_f32_16x16x128_f8f6f4 v[86:89], v[18:25], v[214:221], v[86:89], v204, v204 op_sel_hi:[0,0,0]
	v_mfma_scale_f32_16x16x128_f8f6f4 v[82:85], v[26:33], v[214:221], v[82:85], v204, v204 op_sel_hi:[0,0,0]
	v_mfma_scale_f32_16x16x128_f8f6f4 v[66:69], v[18:25], v[222:229], v[66:69], v204, v204 op_sel_hi:[0,0,0]
	v_mfma_scale_f32_16x16x128_f8f6f4 v[58:61], v[26:33], v[222:229], v[58:61], v204, v204 op_sel_hi:[0,0,0]
	v_mfma_scale_f32_16x16x128_f8f6f4 v[54:57], v[18:25], v[232:239], v[54:57], v204, v204 op_sel_hi:[0,0,0]
	v_mfma_scale_f32_16x16x128_f8f6f4 v[50:53], v[26:33], v[232:239], v[50:53], v204, v204 op_sel_hi:[0,0,0]
	s_setprio 0
	s_setprio 1
	v_mfma_scale_f32_16x16x128_f8f6f4 v[78:81], v[2:9], v[206:213], v[78:81], v204, v204 op_sel_hi:[0,0,0]
	v_mfma_scale_f32_16x16x128_f8f6f4 v[74:77], v[10:17], v[206:213], v[74:77], v204, v204 op_sel_hi:[0,0,0]
	v_mfma_scale_f32_16x16x128_f8f6f4 v[70:73], v[2:9], v[214:221], v[70:73], v204, v204 op_sel_hi:[0,0,0]
	v_mfma_scale_f32_16x16x128_f8f6f4 v[62:65], v[10:17], v[214:221], v[62:65], v204, v204 op_sel_hi:[0,0,0]
	v_mfma_scale_f32_16x16x128_f8f6f4 v[46:49], v[2:9], v[222:229], v[46:49], v204, v204 op_sel_hi:[0,0,0]
	v_mfma_scale_f32_16x16x128_f8f6f4 v[42:45], v[10:17], v[222:229], v[42:45], v204, v204 op_sel_hi:[0,0,0]
	v_mfma_scale_f32_16x16x128_f8f6f4 v[38:41], v[2:9], v[232:239], v[38:41], v204, v204 op_sel_hi:[0,0,0]
	v_mfma_scale_f32_16x16x128_f8f6f4 v[34:37], v[10:17], v[232:239], v[34:37], v204, v204 op_sel_hi:[0,0,0]
	s_setprio 0
	s_add_i32 s18, 0, 0x18000
	s_add_i32 s19, 0, 0x1c000
	s_barrier
	v_add_u32_e32 v14, s18, v198
	v_add_u32_e32 v30, s19, v198
	ds_read_b128 v[2:5], v14
	ds_read_b128 v[6:9], v14 offset:1024
	ds_read_b128 v[10:13], v14 offset:2048
	ds_read_b128 v[14:17], v14 offset:3072
	ds_read_b128 v[18:21], v30
	ds_read_b128 v[22:25], v30 offset:1024
	ds_read_b128 v[26:29], v30 offset:2048
	ds_read_b128 v[30:33], v30 offset:3072
	s_add_u32 s66, s66, 0x40000
	s_addc_u32 s67, s67, 0
	s_mov_b32 m0, s91
	v_lshl_add_u64 v[240:241], s[66:67], 0, v[162:163]
	ds_read_b128 v[206:209], v203 offset:32768
	ds_read_b128 v[210:213], v203 offset:33792
	ds_read_b128 v[214:217], v203 offset:34816
	ds_read_b128 v[218:221], v203 offset:35840
	ds_read_b128 v[222:225], v203 offset:36864
	ds_read_b128 v[226:229], v203 offset:37888
	ds_read_b128 v[232:235], v203 offset:38912
	ds_read_b128 v[236:239], v203 offset:39936
	global_load_lds_dwordx4 v[240:241], off
	v_lshl_add_u64 v[240:241], s[66:67], 0, v[166:167]
	s_mov_b32 m0, s92
	s_nop 0
	global_load_lds_dwordx4 v[240:241], off
	s_waitcnt vmcnt(8)
	s_waitcnt lgkmcnt(0)
	s_barrier
	s_setprio 1
	s_waitcnt lgkmcnt(0)
	v_mfma_scale_f32_16x16x128_f8f6f4 v[158:161], v[2:9], v[206:213], v[158:161], v204, v204 op_sel_hi:[0,0,0]
	v_mfma_scale_f32_16x16x128_f8f6f4 v[154:157], v[10:17], v[206:213], v[154:157], v204, v204 op_sel_hi:[0,0,0]
	v_mfma_scale_f32_16x16x128_f8f6f4 v[150:153], v[2:9], v[214:221], v[150:153], v204, v204 op_sel_hi:[0,0,0]
	v_mfma_scale_f32_16x16x128_f8f6f4 v[146:149], v[10:17], v[214:221], v[146:149], v204, v204 op_sel_hi:[0,0,0]
	v_mfma_scale_f32_16x16x128_f8f6f4 v[130:133], v[2:9], v[222:229], v[130:133], v204, v204 op_sel_hi:[0,0,0]
	v_mfma_scale_f32_16x16x128_f8f6f4 v[122:125], v[10:17], v[222:229], v[122:125], v204, v204 op_sel_hi:[0,0,0]
	v_mfma_scale_f32_16x16x128_f8f6f4 v[118:121], v[2:9], v[232:239], v[118:121], v204, v204 op_sel_hi:[0,0,0]
	v_mfma_scale_f32_16x16x128_f8f6f4 v[114:117], v[10:17], v[232:239], v[114:117], v204, v204 op_sel_hi:[0,0,0]
	s_setprio 0
	s_setprio 1
	v_mfma_scale_f32_16x16x128_f8f6f4 v[142:145], v[18:25], v[206:213], v[142:145], v204, v204 op_sel_hi:[0,0,0]
	v_mfma_scale_f32_16x16x128_f8f6f4 v[138:141], v[26:33], v[206:213], v[138:141], v204, v204 op_sel_hi:[0,0,0]
	v_mfma_scale_f32_16x16x128_f8f6f4 v[134:137], v[18:25], v[214:221], v[134:137], v204, v204 op_sel_hi:[0,0,0]
	v_mfma_scale_f32_16x16x128_f8f6f4 v[126:129], v[26:33], v[214:221], v[126:129], v204, v204 op_sel_hi:[0,0,0]
	v_mfma_scale_f32_16x16x128_f8f6f4 v[110:113], v[18:25], v[222:229], v[110:113], v204, v204 op_sel_hi:[0,0,0]
	v_mfma_scale_f32_16x16x128_f8f6f4 v[106:109], v[26:33], v[222:229], v[106:109], v204, v204 op_sel_hi:[0,0,0]
	v_mfma_scale_f32_16x16x128_f8f6f4 v[102:105], v[18:25], v[232:239], v[102:105], v204, v204 op_sel_hi:[0,0,0]
	v_mfma_scale_f32_16x16x128_f8f6f4 v[98:101], v[26:33], v[232:239], v[98:101], v204, v204 op_sel_hi:[0,0,0]
	s_setprio 0
	s_add_i32 s18, s18, s39
	s_barrier
	v_lshl_add_u64 v[176:177], v[176:177], 0, s[14:15]
	s_mov_b32 m0, s18
	ds_read_b128 v[206:209], v203 offset:49152
	ds_read_b128 v[210:213], v203 offset:50176
	ds_read_b128 v[214:217], v203 offset:51200
	ds_read_b128 v[218:221], v203 offset:52224
	ds_read_b128 v[222:225], v203 offset:53248
	ds_read_b128 v[226:229], v203 offset:54272
	ds_read_b128 v[232:235], v203 offset:55296
	ds_read_b128 v[236:239], v203 offset:56320
	global_load_lds_dwordx4 v[176:177], off
	s_add_i32 m0, s18, 0x2000
	s_add_u32 s62, s62, 0x40080
	v_lshl_add_u64 v[176:177], v[178:179], 0, s[14:15]
	s_addc_u32 s63, s63, 0
	s_add_i32 s18, s19, s39
	global_load_lds_dwordx4 v[176:177], off
	v_lshl_add_u64 v[176:177], s[62:63], 0, v[164:165]
	s_mov_b32 m0, s18
	s_nop 0
	global_load_lds_dwordx4 v[176:177], off
	v_lshl_add_u64 v[176:177], s[62:63], 0, v[168:169]
	s_add_i32 m0, s18, 0x2000
	s_nop 0
	global_load_lds_dwordx4 v[176:177], off
	v_lshl_add_u64 v[176:177], v[180:181], 0, s[14:15]
	s_mov_b32 m0, s93
	s_nop 0
	global_load_lds_dwordx4 v[176:177], off
	v_lshl_add_u64 v[176:177], v[182:183], 0, s[14:15]
	s_mov_b32 m0, s95
	s_nop 0
	global_load_lds_dwordx4 v[176:177], off
	s_waitcnt vmcnt(8)
	s_waitcnt lgkmcnt(0)
	s_barrier
	s_setprio 1
	s_waitcnt lgkmcnt(0)
	v_mfma_scale_f32_16x16x128_f8f6f4 v[94:97], v[2:9], v[206:213], v[94:97], v204, v204 op_sel_hi:[0,0,0]
	v_mfma_scale_f32_16x16x128_f8f6f4 v[90:93], v[10:17], v[206:213], v[90:93], v204, v204 op_sel_hi:[0,0,0]
	v_mfma_scale_f32_16x16x128_f8f6f4 v[86:89], v[2:9], v[214:221], v[86:89], v204, v204 op_sel_hi:[0,0,0]
	v_mfma_scale_f32_16x16x128_f8f6f4 v[82:85], v[10:17], v[214:221], v[82:85], v204, v204 op_sel_hi:[0,0,0]
	v_mfma_scale_f32_16x16x128_f8f6f4 v[66:69], v[2:9], v[222:229], v[66:69], v204, v204 op_sel_hi:[0,0,0]
	v_mfma_scale_f32_16x16x128_f8f6f4 v[58:61], v[10:17], v[222:229], v[58:61], v204, v204 op_sel_hi:[0,0,0]
	v_mfma_scale_f32_16x16x128_f8f6f4 v[54:57], v[2:9], v[232:239], v[54:57], v204, v204 op_sel_hi:[0,0,0]
	v_mfma_scale_f32_16x16x128_f8f6f4 v[50:53], v[10:17], v[232:239], v[50:53], v204, v204 op_sel_hi:[0,0,0]
	s_setprio 0
	s_setprio 1
	v_mfma_scale_f32_16x16x128_f8f6f4 v[78:81], v[18:25], v[206:213], v[78:81], v204, v204 op_sel_hi:[0,0,0]
	v_mfma_scale_f32_16x16x128_f8f6f4 v[74:77], v[26:33], v[206:213], v[74:77], v204, v204 op_sel_hi:[0,0,0]
	v_mfma_scale_f32_16x16x128_f8f6f4 v[70:73], v[18:25], v[214:221], v[70:73], v204, v204 op_sel_hi:[0,0,0]
	v_mfma_scale_f32_16x16x128_f8f6f4 v[62:65], v[26:33], v[214:221], v[62:65], v204, v204 op_sel_hi:[0,0,0]
	v_mfma_scale_f32_16x16x128_f8f6f4 v[46:49], v[18:25], v[222:229], v[46:49], v204, v204 op_sel_hi:[0,0,0]
	v_mfma_scale_f32_16x16x128_f8f6f4 v[42:45], v[26:33], v[222:229], v[42:45], v204, v204 op_sel_hi:[0,0,0]
	v_mfma_scale_f32_16x16x128_f8f6f4 v[38:41], v[18:25], v[232:239], v[38:41], v204, v204 op_sel_hi:[0,0,0]
	v_mfma_scale_f32_16x16x128_f8f6f4 v[34:37], v[26:33], v[232:239], v[34:37], v204, v204 op_sel_hi:[0,0,0]
	s_setprio 0
	s_add_i32 s71, s71, 2
	s_add_u32 s58, s58, 0x100
	s_addc_u32 s59, s59, 0
	s_add_u32 s69, s69, 0x100
	s_addc_u32 s70, s70, 0
	s_cmp_gt_u32 s71, 13
	s_barrier
	s_cbranch_scc0 .LBB0_285
	s_and_b64 vcc, exec, s[16:17]
	s_cbranch_vccz .LBB0_288
	s_barrier

.LBB0_336:
	ds_read_b128 v[142:145], v1
	ds_read_b128 v[152:155], v1 offset:1024
	ds_read_b128 v[156:159], v1 offset:2048
	ds_read_b128 v[160:163], v1 offset:3072
	ds_read_b128 v[164:167], v149
	ds_read_b128 v[168:171], v149 offset:1024
	ds_read_b128 v[172:175], v149 offset:2048
	ds_read_b128 v[176:179], v149 offset:3072
	s_add_u32 s18, s48, 0xfff80080
	s_addc_u32 s19, s49, -1
	s_cmp_eq_u32 s87, 28
	s_cselect_b32 s55, s17, s19
	s_cselect_b32 s54, s56, s18
	s_cselect_b32 s53, s39, s59
	s_cselect_b32 s52, s57, s58
	v_lshl_add_u64 v[212:213], s[48:49], 0, v[138:139]
	s_add_i32 m0, s47, 0xc000
	ds_read_b128 v[180:183], v150
	ds_read_b128 v[184:187], v150 offset:1024
	ds_read_b128 v[188:191], v150 offset:2048
	ds_read_b128 v[192:195], v150 offset:3072
	ds_read_b128 v[196:199], v150 offset:4096
	ds_read_b128 v[200:203], v150 offset:5120
	ds_read_b128 v[204:207], v150 offset:6144
	ds_read_b128 v[208:211], v150 offset:7168
	global_load_lds_dwordx4 v[212:213], off
	v_lshl_add_u64 v[212:213], s[48:49], 0, v[140:141]
	s_add_i32 m0, s47, 0xe000
	s_nop 0
	global_load_lds_dwordx4 v[212:213], off
	s_waitcnt vmcnt(8)
	s_waitcnt lgkmcnt(0)
	s_barrier
	s_setprio 1
	s_waitcnt lgkmcnt(0)
	v_mfma_f32_16x16x32_bf16 v[126:129], v[142:145], v[180:183], v[126:129]
	v_mfma_f32_16x16x32_bf16 v[122:125], v[156:159], v[180:183], v[122:125]
	v_mfma_f32_16x16x32_bf16 v[114:117], v[142:145], v[188:191], v[114:117]
	v_mfma_f32_16x16x32_bf16 v[106:109], v[156:159], v[188:191], v[106:109]
	v_mfma_f32_16x16x32_bf16 v[98:101], v[142:145], v[196:199], v[98:101]
	v_mfma_f32_16x16x32_bf16 v[90:93], v[156:159], v[196:199], v[90:93]
	v_mfma_f32_16x16x32_bf16 v[82:85], v[142:145], v[204:207], v[82:85]
	v_mfma_f32_16x16x32_bf16 v[74:77], v[156:159], v[204:207], v[74:77]
	v_mfma_f32_16x16x32_bf16 v[126:129], v[152:155], v[184:187], v[126:129]
	v_mfma_f32_16x16x32_bf16 v[122:125], v[160:163], v[184:187], v[122:125]
	v_mfma_f32_16x16x32_bf16 v[114:117], v[152:155], v[192:195], v[114:117]
	v_mfma_f32_16x16x32_bf16 v[106:109], v[160:163], v[192:195], v[106:109]
	v_mfma_f32_16x16x32_bf16 v[98:101], v[152:155], v[200:203], v[98:101]
	v_mfma_f32_16x16x32_bf16 v[90:93], v[160:163], v[200:203], v[90:93]
	v_mfma_f32_16x16x32_bf16 v[82:85], v[152:155], v[208:211], v[82:85]
	v_mfma_f32_16x16x32_bf16 v[74:77], v[160:163], v[208:211], v[74:77]
	s_setprio 0
	s_setprio 1
	v_mfma_f32_16x16x32_bf16 v[118:121], v[164:167], v[180:183], v[118:121]
	v_mfma_f32_16x16x32_bf16 v[110:113], v[172:175], v[180:183], v[110:113]
	v_mfma_f32_16x16x32_bf16 v[102:105], v[164:167], v[188:191], v[102:105]
	v_mfma_f32_16x16x32_bf16 v[94:97], v[172:175], v[188:191], v[94:97]
	v_mfma_f32_16x16x32_bf16 v[86:89], v[164:167], v[196:199], v[86:89]
	v_mfma_f32_16x16x32_bf16 v[78:81], v[172:175], v[196:199], v[78:81]
	v_mfma_f32_16x16x32_bf16 v[70:73], v[164:167], v[204:207], v[70:73]
	v_mfma_f32_16x16x32_bf16 v[66:69], v[172:175], v[204:207], v[66:69]
	v_mfma_f32_16x16x32_bf16 v[118:121], v[168:171], v[184:187], v[118:121]
	v_mfma_f32_16x16x32_bf16 v[110:113], v[176:179], v[184:187], v[110:113]
	v_mfma_f32_16x16x32_bf16 v[102:105], v[168:171], v[192:195], v[102:105]
	v_mfma_f32_16x16x32_bf16 v[94:97], v[176:179], v[192:195], v[94:97]
	v_mfma_f32_16x16x32_bf16 v[86:89], v[168:171], v[200:203], v[86:89]
	v_mfma_f32_16x16x32_bf16 v[78:81], v[176:179], v[200:203], v[78:81]
	v_mfma_f32_16x16x32_bf16 v[70:73], v[168:171], v[208:211], v[70:73]
	v_mfma_f32_16x16x32_bf16 v[66:69], v[176:179], v[208:211], v[66:69]
	s_setprio 0
	s_add_i32 s18, s71, s30
	s_barrier
	v_lshl_add_u64 v[212:213], s[52:53], 0, v[132:133]
	s_mov_b32 m0, s18
	ds_read_b128 v[180:183], v150 offset:16384
	ds_read_b128 v[184:187], v150 offset:17408
	ds_read_b128 v[188:191], v150 offset:18432
	ds_read_b128 v[192:195], v150 offset:19456
	ds_read_b128 v[196:199], v150 offset:20480
	ds_read_b128 v[200:203], v150 offset:21504
	ds_read_b128 v[204:207], v150 offset:22528
	ds_read_b128 v[208:211], v150 offset:23552
	global_load_lds_dwordx4 v[212:213], off
	s_add_i32 m0, s18, 0x2000
	s_add_u32 s90, s52, 0x80000
	v_lshl_add_u64 v[214:215], s[52:53], 0, v[136:137]
	s_addc_u32 s91, s53, 0
	s_add_i32 s18, s84, s30
	global_load_lds_dwordx4 v[214:215], off
	v_lshl_add_u64 v[216:217], s[90:91], 0, v[132:133]
	s_mov_b32 m0, s18
	v_lshl_add_u64 v[218:219], s[54:55], 0, v[134:135]
	global_load_lds_dwordx4 v[216:217], off
	v_lshl_add_u64 v[216:217], s[90:91], 0, v[136:137]
	s_add_i32 m0, s18, 0x2000
	s_nop 0
	global_load_lds_dwordx4 v[216:217], off
	v_lshl_add_u64 v[216:217], s[54:55], 0, v[130:131]
	s_mov_b32 m0, s47
	s_nop 0
	global_load_lds_dwordx4 v[216:217], off
	s_mov_b32 m0, s63
	s_nop 0
	global_load_lds_dwordx4 v[218:219], off
	s_waitcnt vmcnt(8)
	s_waitcnt lgkmcnt(0)
	s_barrier
	s_setprio 1
	s_waitcnt lgkmcnt(0)
	v_mfma_f32_16x16x32_bf16 v[62:65], v[142:145], v[180:183], v[62:65]
	v_mfma_f32_16x16x32_bf16 v[58:61], v[156:159], v[180:183], v[58:61]
	v_mfma_f32_16x16x32_bf16 v[50:53], v[142:145], v[188:191], v[50:53]
	v_mfma_f32_16x16x32_bf16 v[42:45], v[156:159], v[188:191], v[42:45]
	v_mfma_f32_16x16x32_bf16 v[34:37], v[142:145], v[196:199], v[34:37]
	v_mfma_f32_16x16x32_bf16 v[26:29], v[156:159], v[196:199], v[26:29]
	v_mfma_f32_16x16x32_bf16 v[18:21], v[142:145], v[204:207], v[18:21]
	v_mfma_f32_16x16x32_bf16 v[10:13], v[156:159], v[204:207], v[10:13]
	v_mfma_f32_16x16x32_bf16 v[62:65], v[152:155], v[184:187], v[62:65]
	v_mfma_f32_16x16x32_bf16 v[58:61], v[160:163], v[184:187], v[58:61]
	v_mfma_f32_16x16x32_bf16 v[50:53], v[152:155], v[192:195], v[50:53]
	v_mfma_f32_16x16x32_bf16 v[42:45], v[160:163], v[192:195], v[42:45]
	v_mfma_f32_16x16x32_bf16 v[34:37], v[152:155], v[200:203], v[34:37]
	v_mfma_f32_16x16x32_bf16 v[26:29], v[160:163], v[200:203], v[26:29]
	v_mfma_f32_16x16x32_bf16 v[18:21], v[152:155], v[208:211], v[18:21]
	v_mfma_f32_16x16x32_bf16 v[10:13], v[160:163], v[208:211], v[10:13]
	s_setprio 0
	s_setprio 1
	v_mfma_f32_16x16x32_bf16 v[54:57], v[164:167], v[180:183], v[54:57]
	v_mfma_f32_16x16x32_bf16 v[46:49], v[172:175], v[180:183], v[46:49]
	v_mfma_f32_16x16x32_bf16 v[38:41], v[164:167], v[188:191], v[38:41]
	v_mfma_f32_16x16x32_bf16 v[30:33], v[172:175], v[188:191], v[30:33]
	v_mfma_f32_16x16x32_bf16 v[22:25], v[164:167], v[196:199], v[22:25]
	v_mfma_f32_16x16x32_bf16 v[14:17], v[172:175], v[196:199], v[14:17]
	v_mfma_f32_16x16x32_bf16 v[6:9], v[164:167], v[204:207], v[6:9]
	v_mfma_f32_16x16x32_bf16 v[2:5], v[172:175], v[204:207], v[2:5]
	v_mfma_f32_16x16x32_bf16 v[54:57], v[168:171], v[184:187], v[54:57]
	v_mfma_f32_16x16x32_bf16 v[46:49], v[176:179], v[184:187], v[46:49]
	v_mfma_f32_16x16x32_bf16 v[38:41], v[168:171], v[192:195], v[38:41]
	v_mfma_f32_16x16x32_bf16 v[30:33], v[176:179], v[192:195], v[30:33]
	v_mfma_f32_16x16x32_bf16 v[22:25], v[168:171], v[200:203], v[22:25]
	v_mfma_f32_16x16x32_bf16 v[14:17], v[176:179], v[200:203], v[14:17]
	v_mfma_f32_16x16x32_bf16 v[6:9], v[168:171], v[208:211], v[6:9]
	v_mfma_f32_16x16x32_bf16 v[2:5], v[176:179], v[208:211], v[2:5]
	s_setprio 0
	s_add_i32 s18, 0, 0x18000
	s_barrier
	v_add_u32_e32 v151, s18, v147
	s_add_i32 s19, 0, 0x1c000
	ds_read_b128 v[142:145], v151
	ds_read_b128 v[152:155], v151 offset:1024
	ds_read_b128 v[156:159], v151 offset:2048
	ds_read_b128 v[160:163], v151 offset:3072
	v_add_u32_e32 v151, s19, v147
	ds_read_b128 v[164:167], v151
	ds_read_b128 v[168:171], v151 offset:1024
	ds_read_b128 v[172:175], v151 offset:2048
	ds_read_b128 v[176:179], v151 offset:3072
	s_add_u32 s54, s54, 0x80000
	s_addc_u32 s55, s55, 0
	s_mov_b32 m0, s66
	v_lshl_add_u64 v[220:221], s[54:55], 0, v[130:131]
	ds_read_b128 v[180:183], v150 offset:32768
	ds_read_b128 v[184:187], v150 offset:33792
	ds_read_b128 v[188:191], v150 offset:34816
	ds_read_b128 v[192:195], v150 offset:35840
	ds_read_b128 v[196:199], v150 offset:36864
	ds_read_b128 v[200:203], v150 offset:37888
	ds_read_b128 v[204:207], v150 offset:38912
	ds_read_b128 v[208:211], v150 offset:39936
	global_load_lds_dwordx4 v[220:221], off
	v_lshl_add_u64 v[220:221], s[54:55], 0, v[134:135]
	s_mov_b32 m0, s67
	s_nop 0
	global_load_lds_dwordx4 v[220:221], off
	s_waitcnt vmcnt(8)
	s_waitcnt lgkmcnt(0)
	s_barrier
	s_setprio 1
	s_waitcnt lgkmcnt(0)
	v_mfma_f32_16x16x32_bf16 v[126:129], v[142:145], v[180:183], v[126:129]
	v_mfma_f32_16x16x32_bf16 v[122:125], v[156:159], v[180:183], v[122:125]
	v_mfma_f32_16x16x32_bf16 v[114:117], v[142:145], v[188:191], v[114:117]
	v_mfma_f32_16x16x32_bf16 v[106:109], v[156:159], v[188:191], v[106:109]
	v_mfma_f32_16x16x32_bf16 v[98:101], v[142:145], v[196:199], v[98:101]
	v_mfma_f32_16x16x32_bf16 v[90:93], v[156:159], v[196:199], v[90:93]
	v_mfma_f32_16x16x32_bf16 v[82:85], v[142:145], v[204:207], v[82:85]
	v_mfma_f32_16x16x32_bf16 v[74:77], v[156:159], v[204:207], v[74:77]
	v_mfma_f32_16x16x32_bf16 v[126:129], v[152:155], v[184:187], v[126:129]
	v_mfma_f32_16x16x32_bf16 v[122:125], v[160:163], v[184:187], v[122:125]
	v_mfma_f32_16x16x32_bf16 v[114:117], v[152:155], v[192:195], v[114:117]
	v_mfma_f32_16x16x32_bf16 v[106:109], v[160:163], v[192:195], v[106:109]
	v_mfma_f32_16x16x32_bf16 v[98:101], v[152:155], v[200:203], v[98:101]
	v_mfma_f32_16x16x32_bf16 v[90:93], v[160:163], v[200:203], v[90:93]
	v_mfma_f32_16x16x32_bf16 v[82:85], v[152:155], v[208:211], v[82:85]
	v_mfma_f32_16x16x32_bf16 v[74:77], v[160:163], v[208:211], v[74:77]
	s_setprio 0
	s_setprio 1
	v_mfma_f32_16x16x32_bf16 v[118:121], v[164:167], v[180:183], v[118:121]
	v_mfma_f32_16x16x32_bf16 v[110:113], v[172:175], v[180:183], v[110:113]
	v_mfma_f32_16x16x32_bf16 v[102:105], v[164:167], v[188:191], v[102:105]
	v_mfma_f32_16x16x32_bf16 v[94:97], v[172:175], v[188:191], v[94:97]
	v_mfma_f32_16x16x32_bf16 v[86:89], v[164:167], v[196:199], v[86:89]
	v_mfma_f32_16x16x32_bf16 v[78:81], v[172:175], v[196:199], v[78:81]
	v_mfma_f32_16x16x32_bf16 v[70:73], v[164:167], v[204:207], v[70:73]
	v_mfma_f32_16x16x32_bf16 v[66:69], v[172:175], v[204:207], v[66:69]
	v_mfma_f32_16x16x32_bf16 v[118:121], v[168:171], v[184:187], v[118:121]
	v_mfma_f32_16x16x32_bf16 v[110:113], v[176:179], v[184:187], v[110:113]
	v_mfma_f32_16x16x32_bf16 v[102:105], v[168:171], v[192:195], v[102:105]
	v_mfma_f32_16x16x32_bf16 v[94:97], v[176:179], v[192:195], v[94:97]
	v_mfma_f32_16x16x32_bf16 v[86:89], v[168:171], v[200:203], v[86:89]
	v_mfma_f32_16x16x32_bf16 v[78:81], v[176:179], v[200:203], v[78:81]
	v_mfma_f32_16x16x32_bf16 v[70:73], v[168:171], v[208:211], v[70:73]
	v_mfma_f32_16x16x32_bf16 v[66:69], v[176:179], v[208:211], v[66:69]
	s_setprio 0
	s_add_i32 s18, s18, s30
	s_barrier
	v_lshl_add_u64 v[212:213], v[212:213], 0, s[12:13]
	s_mov_b32 m0, s18
	ds_read_b128 v[180:183], v150 offset:49152
	ds_read_b128 v[184:187], v150 offset:50176
	ds_read_b128 v[188:191], v150 offset:51200
	ds_read_b128 v[192:195], v150 offset:52224
	ds_read_b128 v[196:199], v150 offset:53248
	ds_read_b128 v[200:203], v150 offset:54272
	ds_read_b128 v[204:207], v150 offset:55296
	ds_read_b128 v[208:211], v150 offset:56320
	global_load_lds_dwordx4 v[212:213], off
	s_add_i32 m0, s18, 0x2000
	s_add_u32 s52, s52, 0x80080
	v_lshl_add_u64 v[212:213], v[214:215], 0, s[12:13]
	s_addc_u32 s53, s53, 0
	s_add_i32 s18, s19, s30
	global_load_lds_dwordx4 v[212:213], off
	v_lshl_add_u64 v[212:213], s[52:53], 0, v[132:133]
	s_mov_b32 m0, s18
	s_nop 0
	global_load_lds_dwordx4 v[212:213], off
	v_lshl_add_u64 v[212:213], s[52:53], 0, v[136:137]
	s_add_i32 m0, s18, 0x2000
	s_nop 0
	global_load_lds_dwordx4 v[212:213], off
	v_lshl_add_u64 v[212:213], v[216:217], 0, s[12:13]
	s_mov_b32 m0, s68
	s_nop 0
	global_load_lds_dwordx4 v[212:213], off
	v_lshl_add_u64 v[212:213], v[218:219], 0, s[12:13]
	s_mov_b32 m0, s69
	s_nop 0
	global_load_lds_dwordx4 v[212:213], off
	s_waitcnt vmcnt(8)
	s_waitcnt lgkmcnt(0)
	s_barrier
	s_setprio 1
	s_waitcnt lgkmcnt(0)
	v_mfma_f32_16x16x32_bf16 v[62:65], v[142:145], v[180:183], v[62:65]
	v_mfma_f32_16x16x32_bf16 v[58:61], v[156:159], v[180:183], v[58:61]
	v_mfma_f32_16x16x32_bf16 v[50:53], v[142:145], v[188:191], v[50:53]
	v_mfma_f32_16x16x32_bf16 v[42:45], v[156:159], v[188:191], v[42:45]
	v_mfma_f32_16x16x32_bf16 v[34:37], v[142:145], v[196:199], v[34:37]
	v_mfma_f32_16x16x32_bf16 v[26:29], v[156:159], v[196:199], v[26:29]
	v_mfma_f32_16x16x32_bf16 v[18:21], v[142:145], v[204:207], v[18:21]
	v_mfma_f32_16x16x32_bf16 v[10:13], v[156:159], v[204:207], v[10:13]
	v_mfma_f32_16x16x32_bf16 v[62:65], v[152:155], v[184:187], v[62:65]
	v_mfma_f32_16x16x32_bf16 v[58:61], v[160:163], v[184:187], v[58:61]
	v_mfma_f32_16x16x32_bf16 v[50:53], v[152:155], v[192:195], v[50:53]
	v_mfma_f32_16x16x32_bf16 v[42:45], v[160:163], v[192:195], v[42:45]
	v_mfma_f32_16x16x32_bf16 v[34:37], v[152:155], v[200:203], v[34:37]
	v_mfma_f32_16x16x32_bf16 v[26:29], v[160:163], v[200:203], v[26:29]
	v_mfma_f32_16x16x32_bf16 v[18:21], v[152:155], v[208:211], v[18:21]
	v_mfma_f32_16x16x32_bf16 v[10:13], v[160:163], v[208:211], v[10:13]
	s_setprio 0
	s_setprio 1
	v_mfma_f32_16x16x32_bf16 v[54:57], v[164:167], v[180:183], v[54:57]
	v_mfma_f32_16x16x32_bf16 v[46:49], v[172:175], v[180:183], v[46:49]
	v_mfma_f32_16x16x32_bf16 v[38:41], v[164:167], v[188:191], v[38:41]
	v_mfma_f32_16x16x32_bf16 v[30:33], v[172:175], v[188:191], v[30:33]
	v_mfma_f32_16x16x32_bf16 v[22:25], v[164:167], v[196:199], v[22:25]
	v_mfma_f32_16x16x32_bf16 v[14:17], v[172:175], v[196:199], v[14:17]
	v_mfma_f32_16x16x32_bf16 v[6:9], v[164:167], v[204:207], v[6:9]
	v_mfma_f32_16x16x32_bf16 v[2:5], v[172:175], v[204:207], v[2:5]
	v_mfma_f32_16x16x32_bf16 v[54:57], v[168:171], v[184:187], v[54:57]
	v_mfma_f32_16x16x32_bf16 v[46:49], v[176:179], v[184:187], v[46:49]
	v_mfma_f32_16x16x32_bf16 v[38:41], v[168:171], v[192:195], v[38:41]
	v_mfma_f32_16x16x32_bf16 v[30:33], v[176:179], v[192:195], v[30:33]
	v_mfma_f32_16x16x32_bf16 v[22:25], v[168:171], v[200:203], v[22:25]
	v_mfma_f32_16x16x32_bf16 v[14:17], v[176:179], v[200:203], v[14:17]
	v_mfma_f32_16x16x32_bf16 v[6:9], v[168:171], v[208:211], v[6:9]
	v_mfma_f32_16x16x32_bf16 v[2:5], v[176:179], v[208:211], v[2:5]
	s_setprio 0
	s_add_i32 s87, s87, 2
	s_add_u32 s48, s48, 0x100
	s_addc_u32 s49, s49, 0
	s_add_u32 s58, s58, 0x100
	s_addc_u32 s59, s59, 0
	s_cmp_gt_u32 s87, 29
	s_barrier
	s_cbranch_scc0 .LBB0_336
	s_and_b64 vcc, exec, s[14:15]
	s_cbranch_vccz .LBB0_339
	s_barrier

.LBB0_846:
	v_add_u32_e32 v2, s77, v162
	ds_read_b128 v[150:153], v2
	ds_read_b128 v[154:157], v2 offset:1024
	ds_read_b128 v[158:161], v2 offset:2048
	ds_read_b128 v[166:169], v2 offset:3072
	v_add_u32_e32 v2, s78, v162
	ds_read_b128 v[170:173], v2
	ds_read_b128 v[174:177], v2 offset:1024
	ds_read_b128 v[178:181], v2 offset:2048
	ds_read_b128 v[182:185], v2 offset:3072
	s_add_u32 s18, s54, 0xfff80080
	s_addc_u32 s19, s55, -1
	s_cmp_eq_u32 s87, 28
	s_cselect_b32 s63, s34, s19
	s_cselect_b32 s62, s35, s18
	s_cselect_b32 s59, s45, s86
	s_cselect_b32 s58, s47, s57
	v_lshl_add_u64 v[4:5], s[54:55], 0, v[142:143]
	s_add_i32 m0, s71, 0xc000
	ds_read_b128 v[186:189], v164
	ds_read_b128 v[190:193], v164 offset:1024
	ds_read_b128 v[194:197], v164 offset:2048
	ds_read_b128 v[198:201], v164 offset:3072
	ds_read_b128 v[202:205], v164 offset:4096
	ds_read_b128 v[206:209], v164 offset:5120
	ds_read_b128 v[210:213], v164 offset:6144
	ds_read_b128 v[214:217], v164 offset:7168
	global_load_lds_dwordx4 v[4:5], off
	v_lshl_add_u64 v[4:5], s[54:55], 0, v[144:145]
	s_add_i32 m0, s71, 0xe000
	s_nop 0
	global_load_lds_dwordx4 v[4:5], off
	s_waitcnt vmcnt(8)
	s_waitcnt lgkmcnt(0)
	s_barrier
	s_setprio 1
	s_waitcnt lgkmcnt(0)
	v_mfma_f32_16x16x32_bf16 v[130:133], v[150:153], v[186:189], v[130:133]
	v_mfma_f32_16x16x32_bf16 v[126:129], v[158:161], v[186:189], v[126:129]
	v_mfma_f32_16x16x32_bf16 v[122:125], v[150:153], v[194:197], v[122:125]
	v_mfma_f32_16x16x32_bf16 v[118:121], v[158:161], v[194:197], v[118:121]
	v_mfma_f32_16x16x32_bf16 v[114:117], v[150:153], v[202:205], v[114:117]
	v_mfma_f32_16x16x32_bf16 v[110:113], v[158:161], v[202:205], v[110:113]
	v_mfma_f32_16x16x32_bf16 v[106:109], v[150:153], v[210:213], v[106:109]
	v_mfma_f32_16x16x32_bf16 v[102:105], v[158:161], v[210:213], v[102:105]
	v_mfma_f32_16x16x32_bf16 v[130:133], v[154:157], v[190:193], v[130:133]
	v_mfma_f32_16x16x32_bf16 v[126:129], v[166:169], v[190:193], v[126:129]
	v_mfma_f32_16x16x32_bf16 v[122:125], v[154:157], v[198:201], v[122:125]
	v_mfma_f32_16x16x32_bf16 v[118:121], v[166:169], v[198:201], v[118:121]
	v_mfma_f32_16x16x32_bf16 v[114:117], v[154:157], v[206:209], v[114:117]
	v_mfma_f32_16x16x32_bf16 v[110:113], v[166:169], v[206:209], v[110:113]
	v_mfma_f32_16x16x32_bf16 v[106:109], v[154:157], v[214:217], v[106:109]
	v_mfma_f32_16x16x32_bf16 v[102:105], v[166:169], v[214:217], v[102:105]
	s_setprio 0
	s_setprio 1
	v_mfma_f32_16x16x32_bf16 v[98:101], v[170:173], v[186:189], v[98:101]
	v_mfma_f32_16x16x32_bf16 v[94:97], v[178:181], v[186:189], v[94:97]
	v_mfma_f32_16x16x32_bf16 v[90:93], v[170:173], v[194:197], v[90:93]
	v_mfma_f32_16x16x32_bf16 v[86:89], v[178:181], v[194:197], v[86:89]
	v_mfma_f32_16x16x32_bf16 v[82:85], v[170:173], v[202:205], v[82:85]
	v_mfma_f32_16x16x32_bf16 v[78:81], v[178:181], v[202:205], v[78:81]
	v_mfma_f32_16x16x32_bf16 v[74:77], v[170:173], v[210:213], v[74:77]
	v_mfma_f32_16x16x32_bf16 v[70:73], v[178:181], v[210:213], v[70:73]
	v_mfma_f32_16x16x32_bf16 v[98:101], v[174:177], v[190:193], v[98:101]
	v_mfma_f32_16x16x32_bf16 v[94:97], v[182:185], v[190:193], v[94:97]
	v_mfma_f32_16x16x32_bf16 v[90:93], v[174:177], v[198:201], v[90:93]
	v_mfma_f32_16x16x32_bf16 v[86:89], v[182:185], v[198:201], v[86:89]
	v_mfma_f32_16x16x32_bf16 v[82:85], v[174:177], v[206:209], v[82:85]
	v_mfma_f32_16x16x32_bf16 v[78:81], v[182:185], v[206:209], v[78:81]
	v_mfma_f32_16x16x32_bf16 v[74:77], v[174:177], v[214:217], v[74:77]
	v_mfma_f32_16x16x32_bf16 v[70:73], v[182:185], v[214:217], v[70:73]
	s_setprio 0
	s_add_i32 s18, s77, s70
	s_barrier
	v_lshl_add_u64 v[218:219], s[58:59], 0, v[136:137]
	s_mov_b32 m0, s18
	ds_read_b128 v[186:189], v164 offset:16384
	ds_read_b128 v[190:193], v164 offset:17408
	ds_read_b128 v[194:197], v164 offset:18432
	ds_read_b128 v[198:201], v164 offset:19456
	ds_read_b128 v[202:205], v164 offset:20480
	ds_read_b128 v[206:209], v164 offset:21504
	ds_read_b128 v[210:213], v164 offset:22528
	ds_read_b128 v[214:217], v164 offset:23552
	global_load_lds_dwordx4 v[218:219], off
	s_add_i32 m0, s18, 0x2000
	s_add_u32 s90, s58, 0x80000
	v_lshl_add_u64 v[220:221], s[58:59], 0, v[140:141]
	s_addc_u32 s91, s59, 0
	s_add_i32 s18, s78, s70
	global_load_lds_dwordx4 v[220:221], off
	v_lshl_add_u64 v[4:5], s[90:91], 0, v[136:137]
	s_mov_b32 m0, s18
	v_lshl_add_u64 v[222:223], s[62:63], 0, v[134:135]
	global_load_lds_dwordx4 v[4:5], off
	v_lshl_add_u64 v[4:5], s[90:91], 0, v[140:141]
	s_add_i32 m0, s18, 0x2000
	v_lshl_add_u64 v[224:225], s[62:63], 0, v[138:139]
	global_load_lds_dwordx4 v[4:5], off
	s_mov_b32 m0, s71
	s_nop 0
	global_load_lds_dwordx4 v[222:223], off
	s_mov_b32 m0, s72
	s_nop 0
	global_load_lds_dwordx4 v[224:225], off
	s_waitcnt vmcnt(8)
	s_waitcnt lgkmcnt(0)
	s_barrier
	s_setprio 1
	s_waitcnt lgkmcnt(0)
	v_mfma_f32_16x16x32_bf16 v[66:69], v[150:153], v[186:189], v[66:69]
	v_mfma_f32_16x16x32_bf16 v[62:65], v[158:161], v[186:189], v[62:65]
	v_mfma_f32_16x16x32_bf16 v[58:61], v[150:153], v[194:197], v[58:61]
	v_mfma_f32_16x16x32_bf16 v[54:57], v[158:161], v[194:197], v[54:57]
	v_mfma_f32_16x16x32_bf16 v[50:53], v[150:153], v[202:205], v[50:53]
	v_mfma_f32_16x16x32_bf16 v[46:49], v[158:161], v[202:205], v[46:49]
	v_mfma_f32_16x16x32_bf16 v[42:45], v[150:153], v[210:213], v[42:45]
	v_mfma_f32_16x16x32_bf16 v[38:41], v[158:161], v[210:213], v[38:41]
	v_mfma_f32_16x16x32_bf16 v[66:69], v[154:157], v[190:193], v[66:69]
	v_mfma_f32_16x16x32_bf16 v[62:65], v[166:169], v[190:193], v[62:65]
	v_mfma_f32_16x16x32_bf16 v[58:61], v[154:157], v[198:201], v[58:61]
	v_mfma_f32_16x16x32_bf16 v[54:57], v[166:169], v[198:201], v[54:57]
	v_mfma_f32_16x16x32_bf16 v[50:53], v[154:157], v[206:209], v[50:53]
	v_mfma_f32_16x16x32_bf16 v[46:49], v[166:169], v[206:209], v[46:49]
	v_mfma_f32_16x16x32_bf16 v[42:45], v[154:157], v[214:217], v[42:45]
	v_mfma_f32_16x16x32_bf16 v[38:41], v[166:169], v[214:217], v[38:41]
	s_setprio 0
	s_setprio 1
	v_mfma_f32_16x16x32_bf16 v[34:37], v[170:173], v[186:189], v[34:37]
	v_mfma_f32_16x16x32_bf16 v[30:33], v[178:181], v[186:189], v[30:33]
	v_mfma_f32_16x16x32_bf16 v[26:29], v[170:173], v[194:197], v[26:29]
	v_mfma_f32_16x16x32_bf16 v[22:25], v[178:181], v[194:197], v[22:25]
	v_mfma_f32_16x16x32_bf16 v[18:21], v[170:173], v[202:205], v[18:21]
	v_mfma_f32_16x16x32_bf16 v[14:17], v[178:181], v[202:205], v[14:17]
	v_mfma_f32_16x16x32_bf16 v[10:13], v[170:173], v[210:213], v[10:13]
	v_mfma_f32_16x16x32_bf16 v[4:7], v[178:181], v[210:213], v[6:9]
	v_mfma_f32_16x16x32_bf16 v[34:37], v[174:177], v[190:193], v[34:37]
	v_mfma_f32_16x16x32_bf16 v[30:33], v[182:185], v[190:193], v[30:33]
	v_mfma_f32_16x16x32_bf16 v[26:29], v[174:177], v[198:201], v[26:29]
	v_mfma_f32_16x16x32_bf16 v[22:25], v[182:185], v[198:201], v[22:25]
	v_mfma_f32_16x16x32_bf16 v[18:21], v[174:177], v[206:209], v[18:21]
	v_mfma_f32_16x16x32_bf16 v[14:17], v[182:185], v[206:209], v[14:17]
	v_mfma_f32_16x16x32_bf16 v[10:13], v[174:177], v[214:217], v[10:13]
	v_mfma_f32_16x16x32_bf16 v[4:7], v[182:185], v[214:217], v[4:7]
	s_setprio 0
	s_add_i32 s18, 0, 0x18000
	s_barrier
	v_add_u32_e32 v2, s18, v162
	s_add_i32 s19, 0, 0x1c000
	ds_read_b128 v[150:153], v2
	ds_read_b128 v[154:157], v2 offset:1024
	ds_read_b128 v[158:161], v2 offset:2048
	ds_read_b128 v[166:169], v2 offset:3072
	v_add_u32_e32 v2, s19, v162
	ds_read_b128 v[170:173], v2
	ds_read_b128 v[174:177], v2 offset:1024
	ds_read_b128 v[178:181], v2 offset:2048
	ds_read_b128 v[182:185], v2 offset:3072
	s_add_u32 s62, s62, 0x80000
	s_addc_u32 s63, s63, 0
	s_mov_b32 m0, s73
	v_lshl_add_u64 v[8:9], s[62:63], 0, v[134:135]
	ds_read_b128 v[186:189], v164 offset:32768
	ds_read_b128 v[190:193], v164 offset:33792
	ds_read_b128 v[194:197], v164 offset:34816
	ds_read_b128 v[198:201], v164 offset:35840
	ds_read_b128 v[202:205], v164 offset:36864
	ds_read_b128 v[206:209], v164 offset:37888
	ds_read_b128 v[210:213], v164 offset:38912
	ds_read_b128 v[214:217], v164 offset:39936
	global_load_lds_dwordx4 v[8:9], off
	v_lshl_add_u64 v[8:9], s[62:63], 0, v[138:139]
	s_mov_b32 m0, s74
	s_nop 0
	global_load_lds_dwordx4 v[8:9], off
	s_waitcnt vmcnt(8)
	s_waitcnt lgkmcnt(0)
	s_barrier
	s_setprio 1
	s_waitcnt lgkmcnt(0)
	v_mfma_f32_16x16x32_bf16 v[130:133], v[150:153], v[186:189], v[130:133]
	v_mfma_f32_16x16x32_bf16 v[126:129], v[158:161], v[186:189], v[126:129]
	v_mfma_f32_16x16x32_bf16 v[122:125], v[150:153], v[194:197], v[122:125]
	v_mfma_f32_16x16x32_bf16 v[118:121], v[158:161], v[194:197], v[118:121]
	v_mfma_f32_16x16x32_bf16 v[114:117], v[150:153], v[202:205], v[114:117]
	v_mfma_f32_16x16x32_bf16 v[110:113], v[158:161], v[202:205], v[110:113]
	v_mfma_f32_16x16x32_bf16 v[106:109], v[150:153], v[210:213], v[106:109]
	v_mfma_f32_16x16x32_bf16 v[102:105], v[158:161], v[210:213], v[102:105]
	v_mfma_f32_16x16x32_bf16 v[130:133], v[154:157], v[190:193], v[130:133]
	v_mfma_f32_16x16x32_bf16 v[126:129], v[166:169], v[190:193], v[126:129]
	v_mfma_f32_16x16x32_bf16 v[122:125], v[154:157], v[198:201], v[122:125]
	v_mfma_f32_16x16x32_bf16 v[118:121], v[166:169], v[198:201], v[118:121]
	v_mfma_f32_16x16x32_bf16 v[114:117], v[154:157], v[206:209], v[114:117]
	v_mfma_f32_16x16x32_bf16 v[110:113], v[166:169], v[206:209], v[110:113]
	v_mfma_f32_16x16x32_bf16 v[106:109], v[154:157], v[214:217], v[106:109]
	v_mfma_f32_16x16x32_bf16 v[102:105], v[166:169], v[214:217], v[102:105]
	s_setprio 0
	s_setprio 1
	v_mfma_f32_16x16x32_bf16 v[98:101], v[170:173], v[186:189], v[98:101]
	v_mfma_f32_16x16x32_bf16 v[94:97], v[178:181], v[186:189], v[94:97]
	v_mfma_f32_16x16x32_bf16 v[90:93], v[170:173], v[194:197], v[90:93]
	v_mfma_f32_16x16x32_bf16 v[86:89], v[178:181], v[194:197], v[86:89]
	v_mfma_f32_16x16x32_bf16 v[82:85], v[170:173], v[202:205], v[82:85]
	v_mfma_f32_16x16x32_bf16 v[78:81], v[178:181], v[202:205], v[78:81]
	v_mfma_f32_16x16x32_bf16 v[74:77], v[170:173], v[210:213], v[74:77]
	v_mfma_f32_16x16x32_bf16 v[70:73], v[178:181], v[210:213], v[70:73]
	v_mfma_f32_16x16x32_bf16 v[98:101], v[174:177], v[190:193], v[98:101]
	v_mfma_f32_16x16x32_bf16 v[94:97], v[182:185], v[190:193], v[94:97]
	v_mfma_f32_16x16x32_bf16 v[90:93], v[174:177], v[198:201], v[90:93]
	v_mfma_f32_16x16x32_bf16 v[86:89], v[182:185], v[198:201], v[86:89]
	v_mfma_f32_16x16x32_bf16 v[82:85], v[174:177], v[206:209], v[82:85]
	v_mfma_f32_16x16x32_bf16 v[78:81], v[182:185], v[206:209], v[78:81]
	v_mfma_f32_16x16x32_bf16 v[74:77], v[174:177], v[214:217], v[74:77]
	v_mfma_f32_16x16x32_bf16 v[70:73], v[182:185], v[214:217], v[70:73]
	s_setprio 0
	s_add_i32 s18, s18, s70
	s_barrier
	v_lshl_add_u64 v[8:9], v[218:219], 0, s[14:15]
	s_mov_b32 m0, s18
	ds_read_b128 v[186:189], v164 offset:49152
	ds_read_b128 v[190:193], v164 offset:50176
	ds_read_b128 v[194:197], v164 offset:51200
	ds_read_b128 v[198:201], v164 offset:52224
	ds_read_b128 v[202:205], v164 offset:53248
	ds_read_b128 v[206:209], v164 offset:54272
	ds_read_b128 v[210:213], v164 offset:55296
	ds_read_b128 v[214:217], v164 offset:56320
	global_load_lds_dwordx4 v[8:9], off
	s_add_i32 m0, s18, 0x2000
	s_add_u32 s58, s58, 0x80080
	v_lshl_add_u64 v[8:9], v[220:221], 0, s[14:15]
	s_addc_u32 s59, s59, 0
	s_add_i32 s18, s19, s70
	global_load_lds_dwordx4 v[8:9], off
	v_lshl_add_u64 v[8:9], s[58:59], 0, v[136:137]
	s_mov_b32 m0, s18
	s_nop 0
	global_load_lds_dwordx4 v[8:9], off
	v_lshl_add_u64 v[8:9], s[58:59], 0, v[140:141]
	s_add_i32 m0, s18, 0x2000
	s_nop 0
	global_load_lds_dwordx4 v[8:9], off
	v_lshl_add_u64 v[8:9], v[222:223], 0, s[14:15]
	s_mov_b32 m0, s75
	s_nop 0
	global_load_lds_dwordx4 v[8:9], off
	v_lshl_add_u64 v[8:9], v[224:225], 0, s[14:15]
	s_mov_b32 m0, s76
	s_nop 0
	global_load_lds_dwordx4 v[8:9], off
	s_waitcnt vmcnt(8)
	s_waitcnt lgkmcnt(0)
	s_barrier
	s_setprio 1
	s_waitcnt lgkmcnt(0)
	v_mfma_f32_16x16x32_bf16 v[66:69], v[150:153], v[186:189], v[66:69]
	v_mfma_f32_16x16x32_bf16 v[62:65], v[158:161], v[186:189], v[62:65]
	v_mfma_f32_16x16x32_bf16 v[58:61], v[150:153], v[194:197], v[58:61]
	v_mfma_f32_16x16x32_bf16 v[54:57], v[158:161], v[194:197], v[54:57]
	v_mfma_f32_16x16x32_bf16 v[50:53], v[150:153], v[202:205], v[50:53]
	v_mfma_f32_16x16x32_bf16 v[46:49], v[158:161], v[202:205], v[46:49]
	v_mfma_f32_16x16x32_bf16 v[42:45], v[150:153], v[210:213], v[42:45]
	v_mfma_f32_16x16x32_bf16 v[38:41], v[158:161], v[210:213], v[38:41]
	v_mfma_f32_16x16x32_bf16 v[66:69], v[154:157], v[190:193], v[66:69]
	v_mfma_f32_16x16x32_bf16 v[62:65], v[166:169], v[190:193], v[62:65]
	v_mfma_f32_16x16x32_bf16 v[58:61], v[154:157], v[198:201], v[58:61]
	v_mfma_f32_16x16x32_bf16 v[54:57], v[166:169], v[198:201], v[54:57]
	v_mfma_f32_16x16x32_bf16 v[50:53], v[154:157], v[206:209], v[50:53]
	v_mfma_f32_16x16x32_bf16 v[46:49], v[166:169], v[206:209], v[46:49]
	v_mfma_f32_16x16x32_bf16 v[42:45], v[154:157], v[214:217], v[42:45]
	v_mfma_f32_16x16x32_bf16 v[38:41], v[166:169], v[214:217], v[38:41]
	s_setprio 0
	s_setprio 1
	v_mfma_f32_16x16x32_bf16 v[34:37], v[170:173], v[186:189], v[34:37]
	v_mfma_f32_16x16x32_bf16 v[30:33], v[178:181], v[186:189], v[30:33]
	v_mfma_f32_16x16x32_bf16 v[26:29], v[170:173], v[194:197], v[26:29]
	v_mfma_f32_16x16x32_bf16 v[22:25], v[178:181], v[194:197], v[22:25]
	v_mfma_f32_16x16x32_bf16 v[18:21], v[170:173], v[202:205], v[18:21]
	v_mfma_f32_16x16x32_bf16 v[14:17], v[178:181], v[202:205], v[14:17]
	v_mfma_f32_16x16x32_bf16 v[8:11], v[170:173], v[210:213], v[10:13]
	v_mfma_f32_16x16x32_bf16 v[4:7], v[178:181], v[210:213], v[4:7]
	v_mfma_f32_16x16x32_bf16 v[34:37], v[174:177], v[190:193], v[34:37]
	v_mfma_f32_16x16x32_bf16 v[30:33], v[182:185], v[190:193], v[30:33]
	v_mfma_f32_16x16x32_bf16 v[26:29], v[174:177], v[198:201], v[26:29]
	v_mfma_f32_16x16x32_bf16 v[22:25], v[182:185], v[198:201], v[22:25]
	v_mfma_f32_16x16x32_bf16 v[18:21], v[174:177], v[206:209], v[18:21]
	v_mfma_f32_16x16x32_bf16 v[14:17], v[182:185], v[206:209], v[14:17]
	v_mfma_f32_16x16x32_bf16 v[10:13], v[174:177], v[214:217], v[8:11]
	v_mfma_f32_16x16x32_bf16 v[6:9], v[182:185], v[214:217], v[4:7]
	s_setprio 0
	s_add_i32 s87, s87, 2
	s_add_u32 s54, s54, 0x100
	s_addc_u32 s55, s55, 0
	s_add_u32 s57, s57, 0x100
	s_addc_u32 s86, s86, 0
	s_cmp_gt_u32 s87, 29
	s_barrier
	s_cbranch_scc0 .LBB0_846
	s_and_b64 vcc, exec, s[16:17]
	s_cbranch_vccz .LBB0_849
	s_barrier

.LBB0_927:
	ds_read_b128 v[130:133], v166
	ds_read_b128 v[134:137], v166 offset:1024
	ds_read_b128 v[138:141], v166 offset:2048
	ds_read_b128 v[142:145], v166 offset:3072
	ds_read_b128 v[170:173], v167
	ds_read_b128 v[174:177], v167 offset:1024
	ds_read_b128 v[178:181], v167 offset:2048
	ds_read_b128 v[182:185], v167 offset:3072
	s_add_u32 s18, s56, 0xfff80080
	s_addc_u32 s19, s57, -1
	s_cmp_eq_u32 s86, 28
	s_cselect_b32 s63, s47, s19
	s_cselect_b32 s62, s82, s18
	s_cselect_b32 s59, s45, s85
	s_cselect_b32 s58, s83, s84
	v_lshl_add_u64 v[162:163], s[56:57], 0, v[154:155]
	s_add_i32 m0, s55, 0xc000
	ds_read_b128 v[186:189], v168
	ds_read_b128 v[190:193], v168 offset:1024
	ds_read_b128 v[194:197], v168 offset:2048
	ds_read_b128 v[198:201], v168 offset:3072
	ds_read_b128 v[202:205], v168 offset:4096
	ds_read_b128 v[206:209], v168 offset:5120
	ds_read_b128 v[210:213], v168 offset:6144
	ds_read_b128 v[214:217], v168 offset:7168
	global_load_lds_dwordx4 v[162:163], off
	v_lshl_add_u64 v[162:163], s[56:57], 0, v[156:157]
	s_add_i32 m0, s55, 0xe000
	s_nop 0
	global_load_lds_dwordx4 v[162:163], off
	s_waitcnt vmcnt(8)
	s_waitcnt lgkmcnt(0)
	s_barrier
	s_setprio 1
	s_waitcnt lgkmcnt(0)
	v_mfma_f32_16x16x32_bf16 v[122:125], v[130:133], v[186:189], v[122:125]
	v_mfma_f32_16x16x32_bf16 v[126:129], v[138:141], v[186:189], v[126:129]
	v_mfma_f32_16x16x32_bf16 v[114:117], v[130:133], v[194:197], v[114:117]
	v_mfma_f32_16x16x32_bf16 v[118:121], v[138:141], v[194:197], v[118:121]
	v_mfma_f32_16x16x32_bf16 v[102:105], v[130:133], v[202:205], v[102:105]
	v_mfma_f32_16x16x32_bf16 v[110:113], v[138:141], v[202:205], v[110:113]
	v_mfma_f32_16x16x32_bf16 v[94:97], v[130:133], v[210:213], v[94:97]
	v_mfma_f32_16x16x32_bf16 v[74:77], v[138:141], v[210:213], v[74:77]
	v_mfma_f32_16x16x32_bf16 v[122:125], v[134:137], v[190:193], v[122:125]
	v_mfma_f32_16x16x32_bf16 v[126:129], v[142:145], v[190:193], v[126:129]
	v_mfma_f32_16x16x32_bf16 v[114:117], v[134:137], v[198:201], v[114:117]
	v_mfma_f32_16x16x32_bf16 v[118:121], v[142:145], v[198:201], v[118:121]
	v_mfma_f32_16x16x32_bf16 v[102:105], v[134:137], v[206:209], v[102:105]
	v_mfma_f32_16x16x32_bf16 v[110:113], v[142:145], v[206:209], v[110:113]
	v_mfma_f32_16x16x32_bf16 v[94:97], v[134:137], v[214:217], v[94:97]
	v_mfma_f32_16x16x32_bf16 v[74:77], v[142:145], v[214:217], v[74:77]
	s_setprio 0
	s_setprio 1
	v_mfma_f32_16x16x32_bf16 v[106:109], v[170:173], v[186:189], v[106:109]
	v_mfma_f32_16x16x32_bf16 v[90:93], v[178:181], v[186:189], v[90:93]
	v_mfma_f32_16x16x32_bf16 v[98:101], v[170:173], v[194:197], v[98:101]
	v_mfma_f32_16x16x32_bf16 v[82:85], v[178:181], v[194:197], v[82:85]
	v_mfma_f32_16x16x32_bf16 v[86:89], v[170:173], v[202:205], v[86:89]
	v_mfma_f32_16x16x32_bf16 v[78:81], v[178:181], v[202:205], v[78:81]
	v_mfma_f32_16x16x32_bf16 v[70:73], v[170:173], v[210:213], v[70:73]
	v_mfma_f32_16x16x32_bf16 v[66:69], v[178:181], v[210:213], v[66:69]
	v_mfma_f32_16x16x32_bf16 v[106:109], v[174:177], v[190:193], v[106:109]
	v_mfma_f32_16x16x32_bf16 v[90:93], v[182:185], v[190:193], v[90:93]
	v_mfma_f32_16x16x32_bf16 v[98:101], v[174:177], v[198:201], v[98:101]
	v_mfma_f32_16x16x32_bf16 v[82:85], v[182:185], v[198:201], v[82:85]
	v_mfma_f32_16x16x32_bf16 v[86:89], v[174:177], v[206:209], v[86:89]
	v_mfma_f32_16x16x32_bf16 v[78:81], v[182:185], v[206:209], v[78:81]
	v_mfma_f32_16x16x32_bf16 v[70:73], v[174:177], v[214:217], v[70:73]
	v_mfma_f32_16x16x32_bf16 v[66:69], v[182:185], v[214:217], v[66:69]
	s_setprio 0
	s_add_i32 s18, s74, s66
	s_barrier
	v_lshl_add_u64 v[162:163], s[58:59], 0, v[148:149]
	s_mov_b32 m0, s18
	ds_read_b128 v[186:189], v168 offset:16384
	ds_read_b128 v[190:193], v168 offset:17408
	ds_read_b128 v[194:197], v168 offset:18432
	ds_read_b128 v[198:201], v168 offset:19456
	ds_read_b128 v[202:205], v168 offset:20480
	ds_read_b128 v[206:209], v168 offset:21504
	ds_read_b128 v[210:213], v168 offset:22528
	ds_read_b128 v[214:217], v168 offset:23552
	global_load_lds_dwordx4 v[162:163], off
	s_add_i32 m0, s18, 0x2000
	s_add_u32 s90, s58, 0x80000
	v_lshl_add_u64 v[218:219], s[58:59], 0, v[152:153]
	s_addc_u32 s91, s59, 0
	s_add_i32 s18, s75, s66
	global_load_lds_dwordx4 v[218:219], off
	v_lshl_add_u64 v[220:221], s[90:91], 0, v[148:149]
	s_mov_b32 m0, s18
	v_lshl_add_u64 v[222:223], s[62:63], 0, v[150:151]
	global_load_lds_dwordx4 v[220:221], off
	v_lshl_add_u64 v[220:221], s[90:91], 0, v[152:153]
	s_add_i32 m0, s18, 0x2000
	s_nop 0
	global_load_lds_dwordx4 v[220:221], off
	v_lshl_add_u64 v[220:221], s[62:63], 0, v[146:147]
	s_mov_b32 m0, s55
	s_nop 0
	global_load_lds_dwordx4 v[220:221], off
	s_mov_b32 m0, s67
	s_nop 0
	global_load_lds_dwordx4 v[222:223], off
	s_waitcnt vmcnt(8)
	s_waitcnt lgkmcnt(0)
	s_barrier
	s_setprio 1
	s_waitcnt lgkmcnt(0)
	v_mfma_f32_16x16x32_bf16 v[62:65], v[130:133], v[186:189], v[62:65]
	v_mfma_f32_16x16x32_bf16 v[58:61], v[138:141], v[186:189], v[58:61]
	v_mfma_f32_16x16x32_bf16 v[50:53], v[130:133], v[194:197], v[50:53]
	v_mfma_f32_16x16x32_bf16 v[42:45], v[138:141], v[194:197], v[42:45]
	v_mfma_f32_16x16x32_bf16 v[34:37], v[130:133], v[202:205], v[34:37]
	v_mfma_f32_16x16x32_bf16 v[26:29], v[138:141], v[202:205], v[26:29]
	v_mfma_f32_16x16x32_bf16 v[18:21], v[130:133], v[210:213], v[18:21]
	v_mfma_f32_16x16x32_bf16 v[10:13], v[138:141], v[210:213], v[10:13]
	v_mfma_f32_16x16x32_bf16 v[62:65], v[134:137], v[190:193], v[62:65]
	v_mfma_f32_16x16x32_bf16 v[58:61], v[142:145], v[190:193], v[58:61]
	v_mfma_f32_16x16x32_bf16 v[50:53], v[134:137], v[198:201], v[50:53]
	v_mfma_f32_16x16x32_bf16 v[42:45], v[142:145], v[198:201], v[42:45]
	v_mfma_f32_16x16x32_bf16 v[34:37], v[134:137], v[206:209], v[34:37]
	v_mfma_f32_16x16x32_bf16 v[26:29], v[142:145], v[206:209], v[26:29]
	v_mfma_f32_16x16x32_bf16 v[18:21], v[134:137], v[214:217], v[18:21]
	v_mfma_f32_16x16x32_bf16 v[10:13], v[142:145], v[214:217], v[10:13]
	s_setprio 0
	s_setprio 1
	v_mfma_f32_16x16x32_bf16 v[54:57], v[170:173], v[186:189], v[54:57]
	v_mfma_f32_16x16x32_bf16 v[46:49], v[178:181], v[186:189], v[46:49]
	v_mfma_f32_16x16x32_bf16 v[38:41], v[170:173], v[194:197], v[38:41]
	v_mfma_f32_16x16x32_bf16 v[30:33], v[178:181], v[194:197], v[30:33]
	v_mfma_f32_16x16x32_bf16 v[22:25], v[170:173], v[202:205], v[22:25]
	v_mfma_f32_16x16x32_bf16 v[14:17], v[178:181], v[202:205], v[14:17]
	v_mfma_f32_16x16x32_bf16 v[6:9], v[170:173], v[210:213], v[6:9]
	v_mfma_f32_16x16x32_bf16 v[2:5], v[178:181], v[210:213], v[2:5]
	v_mfma_f32_16x16x32_bf16 v[54:57], v[174:177], v[190:193], v[54:57]
	v_mfma_f32_16x16x32_bf16 v[46:49], v[182:185], v[190:193], v[46:49]
	v_mfma_f32_16x16x32_bf16 v[38:41], v[174:177], v[198:201], v[38:41]
	v_mfma_f32_16x16x32_bf16 v[30:33], v[182:185], v[198:201], v[30:33]
	v_mfma_f32_16x16x32_bf16 v[22:25], v[174:177], v[206:209], v[22:25]
	v_mfma_f32_16x16x32_bf16 v[14:17], v[182:185], v[206:209], v[14:17]
	v_mfma_f32_16x16x32_bf16 v[6:9], v[174:177], v[214:217], v[6:9]
	v_mfma_f32_16x16x32_bf16 v[2:5], v[182:185], v[214:217], v[2:5]
	s_setprio 0
	s_add_i32 s18, 0, 0x18000
	s_add_i32 s19, 0, 0x1c000
	s_barrier
	v_add_u32_e32 v142, s18, v164
	v_add_u32_e32 v169, s19, v164
	ds_read_b128 v[130:133], v142
	ds_read_b128 v[134:137], v142 offset:1024
	ds_read_b128 v[138:141], v142 offset:2048
	ds_read_b128 v[142:145], v142 offset:3072
	ds_read_b128 v[170:173], v169
	ds_read_b128 v[174:177], v169 offset:1024
	ds_read_b128 v[178:181], v169 offset:2048
	ds_read_b128 v[182:185], v169 offset:3072
	s_add_u32 s62, s62, 0x80000
	s_addc_u32 s63, s63, 0
	s_mov_b32 m0, s68
	v_lshl_add_u64 v[224:225], s[62:63], 0, v[146:147]
	ds_read_b128 v[186:189], v168 offset:32768
	ds_read_b128 v[190:193], v168 offset:33792
	ds_read_b128 v[194:197], v168 offset:34816
	ds_read_b128 v[198:201], v168 offset:35840
	ds_read_b128 v[202:205], v168 offset:36864
	ds_read_b128 v[206:209], v168 offset:37888
	ds_read_b128 v[210:213], v168 offset:38912
	ds_read_b128 v[214:217], v168 offset:39936
	global_load_lds_dwordx4 v[224:225], off
	v_lshl_add_u64 v[224:225], s[62:63], 0, v[150:151]
	s_mov_b32 m0, s69
	s_nop 0
	global_load_lds_dwordx4 v[224:225], off
	s_waitcnt vmcnt(8)
	s_waitcnt lgkmcnt(0)
	s_barrier
	s_setprio 1
	s_waitcnt lgkmcnt(0)
	v_mfma_f32_16x16x32_bf16 v[122:125], v[130:133], v[186:189], v[122:125]
	v_mfma_f32_16x16x32_bf16 v[126:129], v[138:141], v[186:189], v[126:129]
	v_mfma_f32_16x16x32_bf16 v[114:117], v[130:133], v[194:197], v[114:117]
	v_mfma_f32_16x16x32_bf16 v[118:121], v[138:141], v[194:197], v[118:121]
	v_mfma_f32_16x16x32_bf16 v[102:105], v[130:133], v[202:205], v[102:105]
	v_mfma_f32_16x16x32_bf16 v[110:113], v[138:141], v[202:205], v[110:113]
	v_mfma_f32_16x16x32_bf16 v[94:97], v[130:133], v[210:213], v[94:97]
	v_mfma_f32_16x16x32_bf16 v[74:77], v[138:141], v[210:213], v[74:77]
	v_mfma_f32_16x16x32_bf16 v[122:125], v[134:137], v[190:193], v[122:125]
	v_mfma_f32_16x16x32_bf16 v[126:129], v[142:145], v[190:193], v[126:129]
	v_mfma_f32_16x16x32_bf16 v[114:117], v[134:137], v[198:201], v[114:117]
	v_mfma_f32_16x16x32_bf16 v[118:121], v[142:145], v[198:201], v[118:121]
	v_mfma_f32_16x16x32_bf16 v[102:105], v[134:137], v[206:209], v[102:105]
	v_mfma_f32_16x16x32_bf16 v[110:113], v[142:145], v[206:209], v[110:113]
	v_mfma_f32_16x16x32_bf16 v[94:97], v[134:137], v[214:217], v[94:97]
	v_mfma_f32_16x16x32_bf16 v[74:77], v[142:145], v[214:217], v[74:77]
	s_setprio 0
	s_setprio 1
	v_mfma_f32_16x16x32_bf16 v[106:109], v[170:173], v[186:189], v[106:109]
	v_mfma_f32_16x16x32_bf16 v[90:93], v[178:181], v[186:189], v[90:93]
	v_mfma_f32_16x16x32_bf16 v[98:101], v[170:173], v[194:197], v[98:101]
	v_mfma_f32_16x16x32_bf16 v[82:85], v[178:181], v[194:197], v[82:85]
	v_mfma_f32_16x16x32_bf16 v[86:89], v[170:173], v[202:205], v[86:89]
	v_mfma_f32_16x16x32_bf16 v[78:81], v[178:181], v[202:205], v[78:81]
	v_mfma_f32_16x16x32_bf16 v[70:73], v[170:173], v[210:213], v[70:73]
	v_mfma_f32_16x16x32_bf16 v[66:69], v[178:181], v[210:213], v[66:69]
	v_mfma_f32_16x16x32_bf16 v[106:109], v[174:177], v[190:193], v[106:109]
	v_mfma_f32_16x16x32_bf16 v[90:93], v[182:185], v[190:193], v[90:93]
	v_mfma_f32_16x16x32_bf16 v[98:101], v[174:177], v[198:201], v[98:101]
	v_mfma_f32_16x16x32_bf16 v[82:85], v[182:185], v[198:201], v[82:85]
	v_mfma_f32_16x16x32_bf16 v[86:89], v[174:177], v[206:209], v[86:89]
	v_mfma_f32_16x16x32_bf16 v[78:81], v[182:185], v[206:209], v[78:81]
	v_mfma_f32_16x16x32_bf16 v[70:73], v[174:177], v[214:217], v[70:73]
	v_mfma_f32_16x16x32_bf16 v[66:69], v[182:185], v[214:217], v[66:69]
	s_setprio 0
	s_add_i32 s18, s18, s66
	s_barrier
	v_lshl_add_u64 v[162:163], v[162:163], 0, s[12:13]
	s_mov_b32 m0, s18
	ds_read_b128 v[186:189], v168 offset:49152
	ds_read_b128 v[190:193], v168 offset:50176
	ds_read_b128 v[194:197], v168 offset:51200
	ds_read_b128 v[198:201], v168 offset:52224
	ds_read_b128 v[202:205], v168 offset:53248
	ds_read_b128 v[206:209], v168 offset:54272
	ds_read_b128 v[210:213], v168 offset:55296
	ds_read_b128 v[214:217], v168 offset:56320
	global_load_lds_dwordx4 v[162:163], off
	s_add_i32 m0, s18, 0x2000
	s_add_u32 s58, s58, 0x80080
	v_lshl_add_u64 v[162:163], v[218:219], 0, s[12:13]
	s_addc_u32 s59, s59, 0
	s_add_i32 s18, s19, s66
	global_load_lds_dwordx4 v[162:163], off
	v_lshl_add_u64 v[162:163], s[58:59], 0, v[148:149]
	s_mov_b32 m0, s18
	s_nop 0
	global_load_lds_dwordx4 v[162:163], off
	v_lshl_add_u64 v[162:163], s[58:59], 0, v[152:153]
	s_add_i32 m0, s18, 0x2000
	s_nop 0
	global_load_lds_dwordx4 v[162:163], off
	v_lshl_add_u64 v[162:163], v[220:221], 0, s[12:13]
	s_mov_b32 m0, s72
	s_nop 0
	global_load_lds_dwordx4 v[162:163], off
	v_lshl_add_u64 v[162:163], v[222:223], 0, s[12:13]
	s_mov_b32 m0, s73
	s_nop 0
	global_load_lds_dwordx4 v[162:163], off
	s_waitcnt vmcnt(8)
	s_waitcnt lgkmcnt(0)
	s_barrier
	s_setprio 1
	s_waitcnt lgkmcnt(0)
	v_mfma_f32_16x16x32_bf16 v[62:65], v[130:133], v[186:189], v[62:65]
	v_mfma_f32_16x16x32_bf16 v[58:61], v[138:141], v[186:189], v[58:61]
	v_mfma_f32_16x16x32_bf16 v[50:53], v[130:133], v[194:197], v[50:53]
	v_mfma_f32_16x16x32_bf16 v[42:45], v[138:141], v[194:197], v[42:45]
	v_mfma_f32_16x16x32_bf16 v[34:37], v[130:133], v[202:205], v[34:37]
	v_mfma_f32_16x16x32_bf16 v[26:29], v[138:141], v[202:205], v[26:29]
	v_mfma_f32_16x16x32_bf16 v[18:21], v[130:133], v[210:213], v[18:21]
	v_mfma_f32_16x16x32_bf16 v[10:13], v[138:141], v[210:213], v[10:13]
	v_mfma_f32_16x16x32_bf16 v[62:65], v[134:137], v[190:193], v[62:65]
	v_mfma_f32_16x16x32_bf16 v[58:61], v[142:145], v[190:193], v[58:61]
	v_mfma_f32_16x16x32_bf16 v[50:53], v[134:137], v[198:201], v[50:53]
	v_mfma_f32_16x16x32_bf16 v[42:45], v[142:145], v[198:201], v[42:45]
	v_mfma_f32_16x16x32_bf16 v[34:37], v[134:137], v[206:209], v[34:37]
	v_mfma_f32_16x16x32_bf16 v[26:29], v[142:145], v[206:209], v[26:29]
	v_mfma_f32_16x16x32_bf16 v[18:21], v[134:137], v[214:217], v[18:21]
	v_mfma_f32_16x16x32_bf16 v[10:13], v[142:145], v[214:217], v[10:13]
	s_setprio 0
	s_setprio 1
	v_mfma_f32_16x16x32_bf16 v[54:57], v[170:173], v[186:189], v[54:57]
	v_mfma_f32_16x16x32_bf16 v[46:49], v[178:181], v[186:189], v[46:49]
	v_mfma_f32_16x16x32_bf16 v[38:41], v[170:173], v[194:197], v[38:41]
	v_mfma_f32_16x16x32_bf16 v[30:33], v[178:181], v[194:197], v[30:33]
	v_mfma_f32_16x16x32_bf16 v[22:25], v[170:173], v[202:205], v[22:25]
	v_mfma_f32_16x16x32_bf16 v[14:17], v[178:181], v[202:205], v[14:17]
	v_mfma_f32_16x16x32_bf16 v[6:9], v[170:173], v[210:213], v[6:9]
	v_mfma_f32_16x16x32_bf16 v[2:5], v[178:181], v[210:213], v[2:5]
	v_mfma_f32_16x16x32_bf16 v[54:57], v[174:177], v[190:193], v[54:57]
	v_mfma_f32_16x16x32_bf16 v[46:49], v[182:185], v[190:193], v[46:49]
	v_mfma_f32_16x16x32_bf16 v[38:41], v[174:177], v[198:201], v[38:41]
	v_mfma_f32_16x16x32_bf16 v[30:33], v[182:185], v[198:201], v[30:33]
	v_mfma_f32_16x16x32_bf16 v[22:25], v[174:177], v[206:209], v[22:25]
	v_mfma_f32_16x16x32_bf16 v[14:17], v[182:185], v[206:209], v[14:17]
	v_mfma_f32_16x16x32_bf16 v[6:9], v[174:177], v[214:217], v[6:9]
	v_mfma_f32_16x16x32_bf16 v[2:5], v[182:185], v[214:217], v[2:5]
	s_setprio 0
	s_add_i32 s86, s86, 2
	s_add_u32 s56, s56, 0x100
	s_addc_u32 s57, s57, 0
	s_add_u32 s84, s84, 0x100
	s_addc_u32 s85, s85, 0
	s_cmp_gt_u32 s86, 29
	s_barrier
	s_cbranch_scc0 .LBB0_927
	s_and_b64 vcc, exec, s[14:15]
	s_cbranch_vccz .LBB0_930
	s_barrier
